# early combine pass re-mapped over the non-tail workgroups only so the post-barrier remainder is balanced (2 rows per wave)
# speedup vs baseline: 1.0079x; 1.0079x over previous
; #define LAS __attribute__((address_space(3)))
; __device__ __forceinline__ void xcd_barrier(const XcdBarrier& b) {
;     asm volatile("s_waitcnt vmcnt(0)" ::: "memory");
;     __syncthreads();
;     int t_ = threadIdx.x; asm volatile("" : "+v"(t_));
;     if (t_ == 0) {
;         unsigned* bar = b.bar;
;         __builtin_amdgcn_s_waitcnt(0);
;         unsigned nloc = b.st[0], nx = b.st[1];
;         if (nloc == 0u) { xcd_barrier_complete(bar, b.x, b.G, nloc, nx); b.st[0] = nloc; b.st[1] = nx; }
; __device__ __forceinline__ void phase_final(const Ctx& P, volatile LAS int* tab, int vcu, int G) {
;     const int tid = threadIdx.x, lane = tid & 63, wave = __builtin_amdgcn_readfirstlane(tid >> 6);
;     const int gw = vcu * 8 + wave, NGW = G * 8;
;     const float* mod = (const float*)(P.ws + WS_MOD) + (size_t)5 * NMOD; const int* tok = (const int*)(P.ws + WS_TOK); const bf16_t* YB = (const bf16_t*)(P.ws + WS_YB);
;     for (int row = gw; row < ML; row += NGW) {
.LBB0_2648:
	s_or_b64 exec, exec, s[10:11]
	s_cmp_eq_u32 s99, 1
	s_cselect_b32 s98, s8, s98
	s_cmp_eq_u32 s99, 2
	s_cbranch_scc0 .Lseam15
	v_and_b32_e32 v201, 7, v0
	v_lshlrev_b32_e32 v201, 2, v201
	v_add_u32_e32 v201, 0x20144, v201
	ds_read_b32 v202, v201
	s_lshl_b32 s16, s39, 2
	s_waitcnt lgkmcnt(0)
	v_cmp_ge_u32_e32 vcc, s16, v202
	s_nop 1
	s_and_b32 s17, vcc_lo, 0xff
	s_bcnt1_i32_b32 s95, s17
	v_readlane_b32 s18, v202, 7
	s_sub_i32 s18, s18, s16
	s_max_i32 s18, s18, 0
	s_cmp_lt_i32 s98, s18
	s_cbranch_scc1 .Lp16a_tail
	s_mov_b32 s92, s33
	s_mov_b32 s93, s39
	s_sub_i32 s33, s98, s18
	s_sub_i32 s39, s39, s18
	s_mov_b64 s[90:91], s[0:1]
	v_mov_b32_e32 v203, v0
	s_branch .Lp16_body
.Lp16a_tail:
	s_mov_b32 s99, 3
.Lseam15:
	s_mov_b64 s[2:3], s[0:1]
	s_nop 0
	v_mov_b64_e32 v[2:3], s[2:3]
	flat_load_dword v1, v[2:3] offset:296
	s_waitcnt vmcnt(0) lgkmcnt(0)
	v_cmp_gt_i32_e32 vcc, 16, v1
	s_and_saveexec_b64 s[34:35], vcc
	s_cbranch_execz .LBB0_2706
	s_mov_b64 s[2:3], s[0:1]
	s_nop 0
	v_mov_b64_e32 v[2:3], s[2:3]
	flat_load_dword v1, v[2:3] offset:300
	s_waitcnt vmcnt(0) lgkmcnt(0)
	v_cmp_lt_i32_e32 vcc, 15, v1
	s_and_b64 exec, exec, vcc
	s_cbranch_execz .LBB0_2706
	s_mov_b64 s[2:3], s[0:1]
	s_nop 0
	v_mov_b64_e32 v[2:3], s[2:3]
	flat_load_dword v1, v[2:3] offset:296
	s_waitcnt vmcnt(0) lgkmcnt(0)
	v_cmp_gt_i32_e32 vcc, 17, v1
	s_and_b64 exec, exec, vcc
	s_cbranch_execz .LBB0_2706
	s_mov_b64 s[2:3], s[0:1]
	s_nop 0
	v_mov_b64_e32 v[2:3], s[2:3]
	flat_load_dword v1, v[2:3] offset:300
	s_waitcnt vmcnt(0) lgkmcnt(0)
	v_cmp_lt_i32_e32 vcc, 16, v1
	s_and_b64 exec, exec, vcc
	s_cbranch_execz .LBB0_2706
	s_mov_b64 s[4:5], s[0:1]
	s_getreg_b32 s2, hwreg(HW_REG_XCC_ID, 0, 4)
	v_mov_b32_e32 v1, v0
	v_mov_b64_e32 v[2:3], s[4:5]
	flat_load_dword v17, v[2:3] offset:308
	s_waitcnt vmcnt(0)
	s_waitcnt lgkmcnt(0)
	s_barrier
	s_nop 0
	v_cmp_eq_u32_e32 vcc, 0, v1
	s_and_b64 exec, exec, vcc
	s_cbranch_execz .LBB0_2705
	s_add_i32 s3, 0, 0x20020
	v_mov_b32_e32 v1, s3
	s_waitcnt vmcnt(0) expcnt(0) lgkmcnt(0)
	ds_read_b32 v4, v1
	s_add_i32 s3, 0, 0x20024
	v_mov_b32_e32 v1, s3
	ds_read_b32 v2, v1
	s_and_b32 s38, s2, 15
	s_waitcnt lgkmcnt(1)
	v_cmp_ne_u32_e32 vcc, 0, v4
	s_cbranch_vccnz .LBB0_2669
	s_add_u32 s2, s36, 0x1000
	s_addc_u32 s3, s37, 0
	s_add_u32 s4, s36, 0x1100
	s_addc_u32 s5, s37, 0
	s_add_u32 s6, s36, 0x1200
	s_addc_u32 s7, s37, 0
	s_add_u32 s8, s36, 0x1300
	s_addc_u32 s9, s37, 0
	s_mov_b32 s26, 1
	s_mov_b64 s[10:11], 0
	v_mov_b32_e32 v18, 0
	s_branch .LBB0_2657

; #define LAS __attribute__((address_space(3)))
; __device__ __forceinline__ void phase_final(const Ctx& P, volatile LAS int* tab, int vcu, int G) {
;     const int tid = threadIdx.x, lane = tid & 63, wave = __builtin_amdgcn_readfirstlane(tid >> 6);
;     const int gw = vcu * 8 + wave, NGW = G * 8;
;     const float* mod = (const float*)(P.ws + WS_MOD) + (size_t)5 * NMOD; const int* tok = (const int*)(P.ws + WS_TOK); const bf16_t* YB = (const bf16_t*)(P.ws + WS_YB);
;     for (int row = gw; row < ML; row += NGW) {
;         const int e1 = tok[row * 8], pos1 = tok[row * 8 + 1], e2 = tok[row * 8 + 2], pos2 = tok[row * 8 + 3]; const float p1 = ((const float*)tok)[row * 8 + 4], p2 = ((const float*)tok)[row * 8 + 5];
;         const bf16_t* y1 = YB + (size_t)(tab[8 + e1] * 256 + pos1) * DM; const bf16_t* y2 = YB + (size_t)(tab[8 + e2] * 256 + pos2) * DM;
;         const bf16_t* xr = (const bf16_t*)(P.ws + WS_XA) + (size_t)row * DM; const float* g2 = mod + (size_t)(row >> 12) * NMOD + 5 * DM;
.Lp16_tabok:
	v_readfirstlane_b32 s0, v0
	s_lshr_b32 s1, s0, 6
	s_lshl_b32 s3, s33, 3
	s_add_i32 s10, s1, s3
	s_cmpk_gt_i32 s10, 0x3fff
	s_waitcnt lgkmcnt(0)
	s_barrier
	s_cbranch_scc1 .LBB0_2713
	s_mov_b32 s20, 0
	s_mov_b32 s21, 0x7fffffff
	s_cmp_eq_u32 s99, 2
	s_cselect_b32 s21, s95, s21
	s_cmp_eq_u32 s99, 3
	s_cselect_b32 s20, s95, s20
	v_lshlrev_b32_e32 v1, 2, v0
	v_and_b32_e32 v4, 0xfc, v1
	v_mbcnt_lo_u32_b32 v1, -1, 0
	v_mbcnt_hi_u32_b32 v1, -1, v1
	v_and_b32_e32 v5, 64, v1
	v_add_u32_e32 v5, 64, v5
	v_xor_b32_e32 v6, 1, v1
	v_cmp_lt_i32_e32 vcc, v6, v5
	s_lshl_b32 s0, s39, 3
	v_mov_b32_e32 v29, 0
	v_cndmask_b32_e32 v6, v1, v6, vcc
	v_lshlrev_b32_e32 v58, 2, v6
	v_xor_b32_e32 v6, 2, v1
	v_cmp_lt_i32_e32 vcc, v6, v5
	v_lshlrev_b32_e32 v28, 1, v4
	s_add_u32 s11, s36, 0x200000
	v_cndmask_b32_e32 v6, v1, v6, vcc
	v_lshlrev_b32_e32 v59, 2, v6
	v_xor_b32_e32 v6, 4, v1
	v_cmp_lt_i32_e32 vcc, v6, v5
	v_lshl_add_u64 v[20:21], s[36:37], 0, v[28:29]
	s_mov_b64 s[4:5], 0x24ac0000
	v_cndmask_b32_e32 v6, v1, v6, vcc
	v_lshlrev_b32_e32 v60, 2, v6
	v_xor_b32_e32 v6, 8, v1
	v_cmp_lt_i32_e32 vcc, v6, v5
	s_addc_u32 s12, s37, 0
	v_lshl_add_u64 v[30:31], v[20:21], 0, s[4:5]
	v_cndmask_b32_e32 v6, v1, v6, vcc
	v_lshlrev_b32_e32 v61, 2, v6
	v_xor_b32_e32 v6, 16, v1
	v_cmp_lt_i32_e32 vcc, v6, v5
	s_lshl_b32 s2, s33, 6
	s_lshl_b32 s4, s1, 3
	v_cndmask_b32_e32 v6, v1, v6, vcc
	s_add_i32 s2, s2, s4
	s_lshl_b32 s13, s39, 6
	s_ashr_i32 s4, s3, 31
	v_lshlrev_b32_e32 v62, 2, v6
	v_xor_b32_e32 v6, 32, v1
	s_add_u32 s6, s1, s3
	v_cmp_lt_i32_e32 vcc, v6, v5
	s_addc_u32 s7, 0, s4
	s_lshl_b64 s[4:5], s[6:7], 13
	v_cndmask_b32_e32 v1, v1, v6, vcc
	v_and_b32_e32 v5, 63, v0
	v_lshlrev_b32_e32 v63, 2, v1
	v_lshl_or_b32 v0, v5, 4, s4
	v_mov_b32_e32 v1, s5
	s_waitcnt vmcnt(0)
	v_lshl_add_u64 v[0:1], v[2:3], 0, v[0:1]
	s_mov_b64 s[4:5], 0x1000
	s_ashr_i32 s1, s0, 31
	v_lshl_add_u64 v[32:33], v[0:1], 0, s[4:5]
	s_lshl_b64 s[4:5], s[0:1], 13
	s_lshl_b64 s[6:7], s[6:7], 12
	s_add_u32 s6, s36, s6
	v_lshlrev_b32_e32 v28, 3, v5
	s_addc_u32 s7, s37, s7
	v_or_b32_e32 v6, 0x100, v4
	v_or_b32_e32 v8, 0x200, v4
	v_or_b32_e32 v10, 0x300, v4
	v_or_b32_e32 v12, 0x400, v4
	v_or_b32_e32 v14, 0x500, v4
	v_or_b32_e32 v16, 0x600, v4
	v_or_b32_e32 v18, 0x700, v4
	v_lshl_add_u64 v[0:1], s[6:7], 0, v[28:29]
	s_mov_b64 s[6:7], 0x1c2c0800
	v_lshl_add_u64 v[34:35], v[0:1], 0, s[6:7]
	s_lshl_b64 s[6:7], s[0:1], 12
	s_add_i32 s1, 0, 0x20100
	v_lshlrev_b32_e32 v28, 2, v4
	v_lshlrev_b32_e32 v64, 2, v6
	v_lshlrev_b32_e32 v65, 2, v8
	v_lshlrev_b32_e32 v66, 2, v10
	v_lshlrev_b32_e32 v36, 2, v12
	v_mov_b32_e32 v37, v29
	v_lshlrev_b32_e32 v38, 2, v14
	v_mov_b32_e32 v39, v29
	v_lshlrev_b32_e32 v40, 2, v16
	v_mov_b32_e32 v41, v29
	v_lshlrev_b32_e32 v42, 2, v18
	v_mov_b32_e32 v43, v29
	v_mov_b32_e32 v67, 0x358637bd
	v_mov_b64_e32 v[44:45], s[8:9]
	flat_load_dwordx2 v[82:83], v[44:45] offset:272
	s_ashr_i32 s3, s2, 31
	s_lshl_b64 s[8:9], s[2:3], 2
	s_add_u32 s8, s11, s8
	s_addc_u32 s9, s12, s9
	global_load_dwordx4 v[194:197], v29, s[8:9]
	global_load_dwordx2 v[198:199], v29, s[8:9] offset:16
	s_mov_b64 s[14:15], 0x1000
	s_waitcnt vmcnt(2) lgkmcnt(0)
	v_lshl_add_u64 v[82:83], v[82:83], 0, v[28:29]
	v_lshl_add_u64 v[84:85], v[82:83], 0, s[14:15]
	global_load_dwordx4 v[162:165], v[82:83], off
	global_load_dwordx4 v[166:169], v[82:83], off offset:1024
	global_load_dwordx4 v[170:173], v[82:83], off offset:2048
	global_load_dwordx4 v[174:177], v[82:83], off offset:3072
	global_load_dwordx4 v[178:181], v[84:85], off
	global_load_dwordx4 v[182:185], v[84:85], off offset:1024
	global_load_dwordx4 v[186:189], v[84:85], off offset:2048
	global_load_dwordx4 v[190:193], v[84:85], off offset:3072
	s_waitcnt vmcnt(0)

; #define MKCTX() const Ctx P{InTbl{in_tbl()}, (float*)*(__attribute__((address_space(1))) float* const*)((const char*)in_tbl() + offsetof(Params, out)), ws}
; #define IN(k) (((PH_MASK >> (k)) & 1) && KARG_I(ph_lo) <= (k) && (k) < KARG_I(ph_hi))
; #define SEAM(k) do { if (IN(k) && IN((k) + 1)) { XcdBarrier bar_; bar_.bar = (unsigned*)(ws + WS_CTL) + CW_BAR; bar_.x = xb_xcc_id(); bar_.st = MISC + 8; bar_.G = (unsigned)KARG_I(grid); xcd_barrier(bar_); } } while (0)
; __global__ void __launch_bounds__(512, 2) fwd_kernel(Params KP) {
;     ...
;     } SEAM(15);
;     if (IN(16)) { MKCTX(); moe_tables(P, tab, 8); phase_final(P, tab, vcu, G); }
.Lp16a_done:
	s_mov_b32 s99, 3
	s_mov_b64 s[0:1], s[90:91]
	v_mov_b32_e32 v0, v203
	s_mov_b32 s33, s92
	s_mov_b32 s39, s93
	s_waitcnt vmcnt(0) lgkmcnt(0)
	s_branch .Lseam15
